# P8 swiglu epilogue rewritten with packed f32 ops and interleaved chains (bit-identical math); bias loads hoisted to unit loop top
# speedup vs baseline: 1.0196x; 1.0070x over previous
.LBB0_1223:
	s_lshl_b32 s18, s24, 8
	s_and_b32 s28, s18, 0xfffff800
	s_lshl_b32 s18, s24, 7
	s_and_b32 s18, s18, 0x380
	s_add_i32 s28, s28, s18
	s_lshl_b32 s28, s28, 2
	s_add_u32 s28, s51, s28
	s_addc_u32 s29, s52, 0
	s_add_u32 s30, s28, 0x1000
	s_addc_u32 s31, s29, 0
	global_load_dwordx4 v[206:209], v0, s[28:29]
	global_load_dwordx4 v[216:219], v0, s[28:29] offset:16
	global_load_dwordx4 v[224:227], v0, s[30:31]
	global_load_dwordx4 v[228:231], v0, s[30:31] offset:16
	s_add_i32 s60, s60, 1
	v_readlane_b32 s13, v252, 17
	s_mul_i32 s14, s60, s13
	v_readlane_b32 s13, v252, 19
	s_add_i32 s14, s14, s13
	s_ashr_i32 s13, s14, 31
	s_lshr_b32 s13, s13, 29
	s_add_i32 s13, s14, s13
	s_and_b32 s17, s13, -8
	v_readlane_b32 s13, v252, 18
	s_or_b32 s13, s17, s13
	s_cmp_lt_i32 s13, s38
	s_cselect_b64 s[22:23], -1, 0
	s_cmp_ge_i32 s13, s38
	s_cbranch_scc1 .LBB0_1225
	s_sub_i32 s12, s14, s17
	s_lshl_b32 s14, s13, 1
	s_add_i32 s14, s14, 0
	s_add_i32 s14, s14, 0x201e0
	v_mov_b32_e32 v2, s14
	ds_read_u16 v2, v2
	s_mov_b32 s16, s13
	s_waitcnt lgkmcnt(0)
	v_readfirstlane_b32 s14, v2
	s_and_b32 s14, s14, 0xffff
	s_lshl_b32 s14, s14, 3
	s_add_i32 s12, s12, s14

.LBB0_1229:
	s_lshl_b32 s13, s24, 8
	s_and_b32 s26, s13, 0xfffff800
	s_ashr_i32 s27, s26, 31
	s_lshl_b64 s[26:27], s[26:27], 2
	s_add_u32 s13, s51, s26
	s_addc_u32 s17, s52, s27
	s_lshl_b32 s14, s24, 7
	s_and_b32 s14, s14, 0x380
	s_lshl_b32 s24, s14, 2
	s_add_u32 s26, s13, s24
	s_addc_u32 s27, s17, 0
	s_nop 15
	s_nop 3
	v_lshl_add_u64 v[6:7], s[26:27], 0, v[0:1]
	s_mov_b64 s[28:29], 0x1000
	s_movk_i32 s13, 0x1000
	v_lshl_add_u64 v[8:9], v[6:7], 0, s[28:29]
	v_add_co_u32_e32 v6, vcc, s13, v6
	s_mov_b32 s17, 0xc0e00000
	s_nop 0
	v_addc_co_u32_e32 v7, vcc, 0, v7, vcc
	s_nop 0
	v_lshl_add_u32 v20, s25, 8, v170
	v_ashrrev_i32_e32 v21, 31, v20
	v_mov_b32_e32 v27, v1
	s_mov_b32 s13, 0x20000
	s_mov_b64 s[24:25], -1
	s_movk_i32 s66, 0x1800
	s_mov_b32 s64, 0x1f000
	s_mov_b32 s30, 0x3fd9db23
	s_mov_b32 s34, 0xbfb8aa3b
	s_mov_b32 s37, 0
	v_lshlrev_b64 v[18:19], 10, v[20:21]
	v_lshl_add_u64 v[18:19], s[8:9], 0, v[18:19]
	v_lshl_add_u64 v[18:19], v[18:19], 0, s[14:15]
	v_lshl_add_u64 v[18:19], v[18:19], 0, v[162:163]
	v_pk_add_f32 v[154:155], v[154:155], v[206:207]
	v_pk_add_f32 v[156:157], v[156:157], v[208:209]
	v_pk_add_f32 v[146:147], v[146:147], v[216:217]
	v_pk_add_f32 v[148:149], v[148:149], v[218:219]
	v_pk_add_f32 v[158:159], v[158:159], v[224:225]
	v_pk_add_f32 v[160:161], v[160:161], v[226:227]
	v_pk_add_f32 v[150:151], v[150:151], v[228:229]
	v_pk_add_f32 v[152:153], v[152:153], v[230:231]
	v_min_f32_e32 v154, 0x40e00000, v154
	v_min_f32_e32 v155, 0x40e00000, v155
	v_min_f32_e32 v156, 0x40e00000, v156
	v_min_f32_e32 v157, 0x40e00000, v157
	v_min_f32_e32 v146, 0x40e00000, v146
	v_min_f32_e32 v147, 0x40e00000, v147
	v_min_f32_e32 v148, 0x40e00000, v148
	v_min_f32_e32 v149, 0x40e00000, v149
	v_med3_f32 v158, v158, s17, v223
	v_med3_f32 v159, v159, s17, v223
	v_med3_f32 v160, v160, s17, v223
	v_med3_f32 v161, v161, s17, v223
	v_med3_f32 v150, v150, s17, v223
	v_med3_f32 v151, v151, s17, v223
	v_med3_f32 v152, v152, s17, v223
	v_med3_f32 v153, v153, s17, v223
	v_pk_mul_f32 v[24:25], v[154:155], s[30:31] op_sel_hi:[1,0]
	v_pk_mul_f32 v[26:27], v[156:157], s[30:31] op_sel_hi:[1,0]
	v_pk_mul_f32 v[28:29], v[146:147], s[30:31] op_sel_hi:[1,0]
	v_pk_mul_f32 v[30:31], v[148:149], s[30:31] op_sel_hi:[1,0]
	v_pk_mul_f32 v[24:25], v[24:25], s[34:35] op_sel_hi:[1,0]
	v_pk_mul_f32 v[26:27], v[26:27], s[34:35] op_sel_hi:[1,0]
	v_pk_mul_f32 v[28:29], v[28:29], s[34:35] op_sel_hi:[1,0]
	v_pk_mul_f32 v[30:31], v[30:31], s[34:35] op_sel_hi:[1,0]
	v_exp_f32_e32 v24, v24
	v_exp_f32_e32 v25, v25
	v_exp_f32_e32 v26, v26
	v_exp_f32_e32 v27, v27
	v_exp_f32_e32 v28, v28
	v_exp_f32_e32 v29, v29
	v_exp_f32_e32 v30, v30
	v_exp_f32_e32 v31, v31
	v_pk_add_f32 v[24:25], v[24:25], 1.0 op_sel_hi:[1,0]
	v_pk_add_f32 v[26:27], v[26:27], 1.0 op_sel_hi:[1,0]
	v_pk_add_f32 v[28:29], v[28:29], 1.0 op_sel_hi:[1,0]
	v_pk_add_f32 v[30:31], v[30:31], 1.0 op_sel_hi:[1,0]
	v_rcp_f32_e32 v24, v24
	v_rcp_f32_e32 v25, v25
	v_rcp_f32_e32 v26, v26
	v_rcp_f32_e32 v27, v27
	v_rcp_f32_e32 v28, v28
	v_rcp_f32_e32 v29, v29
	v_rcp_f32_e32 v30, v30
	v_rcp_f32_e32 v31, v31
	v_pk_add_f32 v[158:159], v[158:159], 1.0 op_sel_hi:[1,0]
	v_pk_add_f32 v[160:161], v[160:161], 1.0 op_sel_hi:[1,0]
	v_pk_add_f32 v[150:151], v[150:151], 1.0 op_sel_hi:[1,0]
	v_pk_add_f32 v[152:153], v[152:153], 1.0 op_sel_hi:[1,0]
	v_pk_mul_f32 v[154:155], v[154:155], v[24:25]
	v_pk_mul_f32 v[156:157], v[156:157], v[26:27]
	v_pk_mul_f32 v[146:147], v[146:147], v[28:29]
	v_pk_mul_f32 v[148:149], v[148:149], v[30:31]
	v_pk_mul_f32 v[154:155], v[158:159], v[154:155]
	v_pk_mul_f32 v[156:157], v[160:161], v[156:157]
	v_pk_mul_f32 v[146:147], v[150:151], v[146:147]
	v_pk_mul_f32 v[148:149], v[152:153], v[148:149]
	v_cvt_pk_fp8_f32 v32, v154, v155
	v_cvt_pk_fp8_f32 v33, v146, v147
	v_cvt_pk_fp8_f32 v32, v156, v157 op_sel:[0,0,1]
	v_cvt_pk_fp8_f32 v33, v148, v149 op_sel:[0,0,1]
	s_nop 0
	global_store_dwordx2 v[18:19], v[32:33], off
	v_pk_add_f32 v[138:139], v[138:139], v[206:207]
	v_pk_add_f32 v[140:141], v[140:141], v[208:209]
	v_pk_add_f32 v[130:131], v[130:131], v[216:217]
	v_pk_add_f32 v[132:133], v[132:133], v[218:219]
	v_pk_add_f32 v[142:143], v[142:143], v[224:225]
	v_pk_add_f32 v[144:145], v[144:145], v[226:227]
	v_pk_add_f32 v[134:135], v[134:135], v[228:229]
	v_pk_add_f32 v[136:137], v[136:137], v[230:231]
	v_min_f32_e32 v138, 0x40e00000, v138
	v_min_f32_e32 v139, 0x40e00000, v139
	v_min_f32_e32 v140, 0x40e00000, v140
	v_min_f32_e32 v141, 0x40e00000, v141
	v_min_f32_e32 v130, 0x40e00000, v130
	v_min_f32_e32 v131, 0x40e00000, v131
	v_min_f32_e32 v132, 0x40e00000, v132
	v_min_f32_e32 v133, 0x40e00000, v133
	v_med3_f32 v142, v142, s17, v223
	v_med3_f32 v143, v143, s17, v223
	v_med3_f32 v144, v144, s17, v223
	v_med3_f32 v145, v145, s17, v223
	v_med3_f32 v134, v134, s17, v223
	v_med3_f32 v135, v135, s17, v223
	v_med3_f32 v136, v136, s17, v223
	v_med3_f32 v137, v137, s17, v223
	v_pk_mul_f32 v[24:25], v[138:139], s[30:31] op_sel_hi:[1,0]
	v_pk_mul_f32 v[26:27], v[140:141], s[30:31] op_sel_hi:[1,0]
	v_pk_mul_f32 v[28:29], v[130:131], s[30:31] op_sel_hi:[1,0]
	v_pk_mul_f32 v[30:31], v[132:133], s[30:31] op_sel_hi:[1,0]
	v_pk_mul_f32 v[24:25], v[24:25], s[34:35] op_sel_hi:[1,0]
	v_pk_mul_f32 v[26:27], v[26:27], s[34:35] op_sel_hi:[1,0]
	v_pk_mul_f32 v[28:29], v[28:29], s[34:35] op_sel_hi:[1,0]
	v_pk_mul_f32 v[30:31], v[30:31], s[34:35] op_sel_hi:[1,0]
	v_exp_f32_e32 v24, v24
	v_exp_f32_e32 v25, v25
	v_exp_f32_e32 v26, v26
	v_exp_f32_e32 v27, v27
	v_exp_f32_e32 v28, v28
	v_exp_f32_e32 v29, v29
	v_exp_f32_e32 v30, v30
	v_exp_f32_e32 v31, v31
	v_pk_add_f32 v[24:25], v[24:25], 1.0 op_sel_hi:[1,0]
	v_pk_add_f32 v[26:27], v[26:27], 1.0 op_sel_hi:[1,0]
	v_pk_add_f32 v[28:29], v[28:29], 1.0 op_sel_hi:[1,0]
	v_pk_add_f32 v[30:31], v[30:31], 1.0 op_sel_hi:[1,0]
	v_rcp_f32_e32 v24, v24
	v_rcp_f32_e32 v25, v25
	v_rcp_f32_e32 v26, v26
	v_rcp_f32_e32 v27, v27
	v_rcp_f32_e32 v28, v28
	v_rcp_f32_e32 v29, v29
	v_rcp_f32_e32 v30, v30
	v_rcp_f32_e32 v31, v31
	v_pk_add_f32 v[142:143], v[142:143], 1.0 op_sel_hi:[1,0]
	v_pk_add_f32 v[144:145], v[144:145], 1.0 op_sel_hi:[1,0]
	v_pk_add_f32 v[134:135], v[134:135], 1.0 op_sel_hi:[1,0]
	v_pk_add_f32 v[136:137], v[136:137], 1.0 op_sel_hi:[1,0]
	v_pk_mul_f32 v[138:139], v[138:139], v[24:25]
	v_pk_mul_f32 v[140:141], v[140:141], v[26:27]
	v_pk_mul_f32 v[130:131], v[130:131], v[28:29]
	v_pk_mul_f32 v[132:133], v[132:133], v[30:31]
	v_pk_mul_f32 v[138:139], v[142:143], v[138:139]
	v_pk_mul_f32 v[140:141], v[144:145], v[140:141]
	v_pk_mul_f32 v[130:131], v[134:135], v[130:131]
	v_pk_mul_f32 v[132:133], v[136:137], v[132:133]
	v_cvt_pk_fp8_f32 v32, v138, v139
	v_cvt_pk_fp8_f32 v33, v130, v131
	v_cvt_pk_fp8_f32 v32, v140, v141 op_sel:[0,0,1]
	v_cvt_pk_fp8_f32 v33, v132, v133 op_sel:[0,0,1]
	s_mov_b32 s36, 0x4000
	v_lshl_add_u64 v[22:23], v[18:19], 0, s[36:37]
	global_store_dwordx2 v[22:23], v[32:33], off
	v_pk_add_f32 v[122:123], v[122:123], v[206:207]
	v_pk_add_f32 v[124:125], v[124:125], v[208:209]
	v_pk_add_f32 v[114:115], v[114:115], v[216:217]
	v_pk_add_f32 v[116:117], v[116:117], v[218:219]
	v_pk_add_f32 v[126:127], v[126:127], v[224:225]
	v_pk_add_f32 v[128:129], v[128:129], v[226:227]
	v_pk_add_f32 v[118:119], v[118:119], v[228:229]
	v_pk_add_f32 v[120:121], v[120:121], v[230:231]
	v_min_f32_e32 v122, 0x40e00000, v122
	v_min_f32_e32 v123, 0x40e00000, v123
	v_min_f32_e32 v124, 0x40e00000, v124
	v_min_f32_e32 v125, 0x40e00000, v125
	v_min_f32_e32 v114, 0x40e00000, v114
	v_min_f32_e32 v115, 0x40e00000, v115
	v_min_f32_e32 v116, 0x40e00000, v116
	v_min_f32_e32 v117, 0x40e00000, v117
	v_med3_f32 v126, v126, s17, v223
	v_med3_f32 v127, v127, s17, v223
	v_med3_f32 v128, v128, s17, v223
	v_med3_f32 v129, v129, s17, v223
	v_med3_f32 v118, v118, s17, v223
	v_med3_f32 v119, v119, s17, v223
	v_med3_f32 v120, v120, s17, v223
	v_med3_f32 v121, v121, s17, v223
	v_pk_mul_f32 v[24:25], v[122:123], s[30:31] op_sel_hi:[1,0]
	v_pk_mul_f32 v[26:27], v[124:125], s[30:31] op_sel_hi:[1,0]
	v_pk_mul_f32 v[28:29], v[114:115], s[30:31] op_sel_hi:[1,0]
	v_pk_mul_f32 v[30:31], v[116:117], s[30:31] op_sel_hi:[1,0]
	v_pk_mul_f32 v[24:25], v[24:25], s[34:35] op_sel_hi:[1,0]
	v_pk_mul_f32 v[26:27], v[26:27], s[34:35] op_sel_hi:[1,0]
	v_pk_mul_f32 v[28:29], v[28:29], s[34:35] op_sel_hi:[1,0]
	v_pk_mul_f32 v[30:31], v[30:31], s[34:35] op_sel_hi:[1,0]
	v_exp_f32_e32 v24, v24
	v_exp_f32_e32 v25, v25
	v_exp_f32_e32 v26, v26
	v_exp_f32_e32 v27, v27
	v_exp_f32_e32 v28, v28
	v_exp_f32_e32 v29, v29
	v_exp_f32_e32 v30, v30
	v_exp_f32_e32 v31, v31
	v_pk_add_f32 v[24:25], v[24:25], 1.0 op_sel_hi:[1,0]
	v_pk_add_f32 v[26:27], v[26:27], 1.0 op_sel_hi:[1,0]
	v_pk_add_f32 v[28:29], v[28:29], 1.0 op_sel_hi:[1,0]
	v_pk_add_f32 v[30:31], v[30:31], 1.0 op_sel_hi:[1,0]
	v_rcp_f32_e32 v24, v24
	v_rcp_f32_e32 v25, v25
	v_rcp_f32_e32 v26, v26
	v_rcp_f32_e32 v27, v27
	v_rcp_f32_e32 v28, v28
	v_rcp_f32_e32 v29, v29
	v_rcp_f32_e32 v30, v30
	v_rcp_f32_e32 v31, v31
	v_pk_add_f32 v[126:127], v[126:127], 1.0 op_sel_hi:[1,0]
	v_pk_add_f32 v[128:129], v[128:129], 1.0 op_sel_hi:[1,0]
	v_pk_add_f32 v[118:119], v[118:119], 1.0 op_sel_hi:[1,0]
	v_pk_add_f32 v[120:121], v[120:121], 1.0 op_sel_hi:[1,0]
	v_pk_mul_f32 v[122:123], v[122:123], v[24:25]
	v_pk_mul_f32 v[124:125], v[124:125], v[26:27]
	v_pk_mul_f32 v[114:115], v[114:115], v[28:29]
	v_pk_mul_f32 v[116:117], v[116:117], v[30:31]
	v_pk_mul_f32 v[122:123], v[126:127], v[122:123]
	v_pk_mul_f32 v[124:125], v[128:129], v[124:125]
	v_pk_mul_f32 v[114:115], v[118:119], v[114:115]
	v_pk_mul_f32 v[116:117], v[120:121], v[116:117]
	v_cvt_pk_fp8_f32 v32, v122, v123
	v_cvt_pk_fp8_f32 v33, v114, v115
	v_cvt_pk_fp8_f32 v32, v124, v125 op_sel:[0,0,1]
	v_cvt_pk_fp8_f32 v33, v116, v117 op_sel:[0,0,1]
	s_mov_b32 s36, 0x8000
	v_lshl_add_u64 v[22:23], v[18:19], 0, s[36:37]
	global_store_dwordx2 v[22:23], v[32:33], off
	v_pk_add_f32 v[106:107], v[106:107], v[206:207]
	v_pk_add_f32 v[108:109], v[108:109], v[208:209]
	v_pk_add_f32 v[98:99], v[98:99], v[216:217]
	v_pk_add_f32 v[100:101], v[100:101], v[218:219]
	v_pk_add_f32 v[110:111], v[110:111], v[224:225]
	v_pk_add_f32 v[112:113], v[112:113], v[226:227]
	v_pk_add_f32 v[102:103], v[102:103], v[228:229]
	v_pk_add_f32 v[104:105], v[104:105], v[230:231]
	v_min_f32_e32 v106, 0x40e00000, v106
	v_min_f32_e32 v107, 0x40e00000, v107
	v_min_f32_e32 v108, 0x40e00000, v108
	v_min_f32_e32 v109, 0x40e00000, v109
	v_min_f32_e32 v98, 0x40e00000, v98
	v_min_f32_e32 v99, 0x40e00000, v99
	v_min_f32_e32 v100, 0x40e00000, v100
	v_min_f32_e32 v101, 0x40e00000, v101
	v_med3_f32 v110, v110, s17, v223
	v_med3_f32 v111, v111, s17, v223
	v_med3_f32 v112, v112, s17, v223
	v_med3_f32 v113, v113, s17, v223
	v_med3_f32 v102, v102, s17, v223
	v_med3_f32 v103, v103, s17, v223
	v_med3_f32 v104, v104, s17, v223
	v_med3_f32 v105, v105, s17, v223
	v_pk_mul_f32 v[24:25], v[106:107], s[30:31] op_sel_hi:[1,0]
	v_pk_mul_f32 v[26:27], v[108:109], s[30:31] op_sel_hi:[1,0]
	v_pk_mul_f32 v[28:29], v[98:99], s[30:31] op_sel_hi:[1,0]
	v_pk_mul_f32 v[30:31], v[100:101], s[30:31] op_sel_hi:[1,0]
	v_pk_mul_f32 v[24:25], v[24:25], s[34:35] op_sel_hi:[1,0]
	v_pk_mul_f32 v[26:27], v[26:27], s[34:35] op_sel_hi:[1,0]
	v_pk_mul_f32 v[28:29], v[28:29], s[34:35] op_sel_hi:[1,0]
	v_pk_mul_f32 v[30:31], v[30:31], s[34:35] op_sel_hi:[1,0]
	v_exp_f32_e32 v24, v24
	v_exp_f32_e32 v25, v25
	v_exp_f32_e32 v26, v26
	v_exp_f32_e32 v27, v27
	v_exp_f32_e32 v28, v28
	v_exp_f32_e32 v29, v29
	v_exp_f32_e32 v30, v30
	v_exp_f32_e32 v31, v31
	v_pk_add_f32 v[24:25], v[24:25], 1.0 op_sel_hi:[1,0]
	v_pk_add_f32 v[26:27], v[26:27], 1.0 op_sel_hi:[1,0]
	v_pk_add_f32 v[28:29], v[28:29], 1.0 op_sel_hi:[1,0]
	v_pk_add_f32 v[30:31], v[30:31], 1.0 op_sel_hi:[1,0]
	v_rcp_f32_e32 v24, v24
	v_rcp_f32_e32 v25, v25
	v_rcp_f32_e32 v26, v26
	v_rcp_f32_e32 v27, v27
	v_rcp_f32_e32 v28, v28
	v_rcp_f32_e32 v29, v29
	v_rcp_f32_e32 v30, v30
	v_rcp_f32_e32 v31, v31
	v_pk_add_f32 v[110:111], v[110:111], 1.0 op_sel_hi:[1,0]
	v_pk_add_f32 v[112:113], v[112:113], 1.0 op_sel_hi:[1,0]
	v_pk_add_f32 v[102:103], v[102:103], 1.0 op_sel_hi:[1,0]
	v_pk_add_f32 v[104:105], v[104:105], 1.0 op_sel_hi:[1,0]
	v_pk_mul_f32 v[106:107], v[106:107], v[24:25]
	v_pk_mul_f32 v[108:109], v[108:109], v[26:27]
	v_pk_mul_f32 v[98:99], v[98:99], v[28:29]
	v_pk_mul_f32 v[100:101], v[100:101], v[30:31]
	v_pk_mul_f32 v[106:107], v[110:111], v[106:107]
	v_pk_mul_f32 v[108:109], v[112:113], v[108:109]
	v_pk_mul_f32 v[98:99], v[102:103], v[98:99]
	v_pk_mul_f32 v[100:101], v[104:105], v[100:101]
	v_cvt_pk_fp8_f32 v32, v106, v107
	v_cvt_pk_fp8_f32 v33, v98, v99
	v_cvt_pk_fp8_f32 v32, v108, v109 op_sel:[0,0,1]
	v_cvt_pk_fp8_f32 v33, v100, v101 op_sel:[0,0,1]
	s_mov_b32 s36, 0xc000
	v_lshl_add_u64 v[22:23], v[18:19], 0, s[36:37]
	global_store_dwordx2 v[22:23], v[32:33], off
	v_pk_add_f32 v[90:91], v[90:91], v[206:207]
	v_pk_add_f32 v[92:93], v[92:93], v[208:209]
	v_pk_add_f32 v[82:83], v[82:83], v[216:217]
	v_pk_add_f32 v[84:85], v[84:85], v[218:219]
	v_pk_add_f32 v[94:95], v[94:95], v[224:225]
	v_pk_add_f32 v[96:97], v[96:97], v[226:227]
	v_pk_add_f32 v[86:87], v[86:87], v[228:229]
	v_pk_add_f32 v[88:89], v[88:89], v[230:231]
	v_min_f32_e32 v90, 0x40e00000, v90
	v_min_f32_e32 v91, 0x40e00000, v91
	v_min_f32_e32 v92, 0x40e00000, v92
	v_min_f32_e32 v93, 0x40e00000, v93
	v_min_f32_e32 v82, 0x40e00000, v82
	v_min_f32_e32 v83, 0x40e00000, v83
	v_min_f32_e32 v84, 0x40e00000, v84
	v_min_f32_e32 v85, 0x40e00000, v85
	v_med3_f32 v94, v94, s17, v223
	v_med3_f32 v95, v95, s17, v223
	v_med3_f32 v96, v96, s17, v223
	v_med3_f32 v97, v97, s17, v223
	v_med3_f32 v86, v86, s17, v223
	v_med3_f32 v87, v87, s17, v223
	v_med3_f32 v88, v88, s17, v223
	v_med3_f32 v89, v89, s17, v223
	v_pk_mul_f32 v[24:25], v[90:91], s[30:31] op_sel_hi:[1,0]
	v_pk_mul_f32 v[26:27], v[92:93], s[30:31] op_sel_hi:[1,0]
	v_pk_mul_f32 v[28:29], v[82:83], s[30:31] op_sel_hi:[1,0]
	v_pk_mul_f32 v[30:31], v[84:85], s[30:31] op_sel_hi:[1,0]
	v_pk_mul_f32 v[24:25], v[24:25], s[34:35] op_sel_hi:[1,0]
	v_pk_mul_f32 v[26:27], v[26:27], s[34:35] op_sel_hi:[1,0]
	v_pk_mul_f32 v[28:29], v[28:29], s[34:35] op_sel_hi:[1,0]
	v_pk_mul_f32 v[30:31], v[30:31], s[34:35] op_sel_hi:[1,0]
	v_exp_f32_e32 v24, v24
	v_exp_f32_e32 v25, v25
	v_exp_f32_e32 v26, v26
	v_exp_f32_e32 v27, v27
	v_exp_f32_e32 v28, v28
	v_exp_f32_e32 v29, v29
	v_exp_f32_e32 v30, v30
	v_exp_f32_e32 v31, v31
	v_pk_add_f32 v[24:25], v[24:25], 1.0 op_sel_hi:[1,0]
	v_pk_add_f32 v[26:27], v[26:27], 1.0 op_sel_hi:[1,0]
	v_pk_add_f32 v[28:29], v[28:29], 1.0 op_sel_hi:[1,0]
	v_pk_add_f32 v[30:31], v[30:31], 1.0 op_sel_hi:[1,0]
	v_rcp_f32_e32 v24, v24
	v_rcp_f32_e32 v25, v25
	v_rcp_f32_e32 v26, v26
	v_rcp_f32_e32 v27, v27
	v_rcp_f32_e32 v28, v28
	v_rcp_f32_e32 v29, v29
	v_rcp_f32_e32 v30, v30
	v_rcp_f32_e32 v31, v31
	v_pk_add_f32 v[94:95], v[94:95], 1.0 op_sel_hi:[1,0]
	v_pk_add_f32 v[96:97], v[96:97], 1.0 op_sel_hi:[1,0]
	v_pk_add_f32 v[86:87], v[86:87], 1.0 op_sel_hi:[1,0]
	v_pk_add_f32 v[88:89], v[88:89], 1.0 op_sel_hi:[1,0]
	v_pk_mul_f32 v[90:91], v[90:91], v[24:25]
	v_pk_mul_f32 v[92:93], v[92:93], v[26:27]
	v_pk_mul_f32 v[82:83], v[82:83], v[28:29]
	v_pk_mul_f32 v[84:85], v[84:85], v[30:31]
	v_pk_mul_f32 v[90:91], v[94:95], v[90:91]
	v_pk_mul_f32 v[92:93], v[96:97], v[92:93]
	v_pk_mul_f32 v[82:83], v[86:87], v[82:83]
	v_pk_mul_f32 v[84:85], v[88:89], v[84:85]
	v_cvt_pk_fp8_f32 v32, v90, v91
	v_cvt_pk_fp8_f32 v33, v82, v83
	v_cvt_pk_fp8_f32 v32, v92, v93 op_sel:[0,0,1]
	v_cvt_pk_fp8_f32 v33, v84, v85 op_sel:[0,0,1]
	s_mov_b32 s36, 0x20000
	v_lshl_add_u64 v[22:23], v[18:19], 0, s[36:37]
	global_store_dwordx2 v[22:23], v[32:33], off
	v_pk_add_f32 v[74:75], v[74:75], v[206:207]
	v_pk_add_f32 v[76:77], v[76:77], v[208:209]
	v_pk_add_f32 v[66:67], v[66:67], v[216:217]
	v_pk_add_f32 v[68:69], v[68:69], v[218:219]
	v_pk_add_f32 v[78:79], v[78:79], v[224:225]
	v_pk_add_f32 v[80:81], v[80:81], v[226:227]
	v_pk_add_f32 v[70:71], v[70:71], v[228:229]
	v_pk_add_f32 v[72:73], v[72:73], v[230:231]
	v_min_f32_e32 v74, 0x40e00000, v74
	v_min_f32_e32 v75, 0x40e00000, v75
	v_min_f32_e32 v76, 0x40e00000, v76
	v_min_f32_e32 v77, 0x40e00000, v77
	v_min_f32_e32 v66, 0x40e00000, v66
	v_min_f32_e32 v67, 0x40e00000, v67
	v_min_f32_e32 v68, 0x40e00000, v68
	v_min_f32_e32 v69, 0x40e00000, v69
	v_med3_f32 v78, v78, s17, v223
	v_med3_f32 v79, v79, s17, v223
	v_med3_f32 v80, v80, s17, v223
	v_med3_f32 v81, v81, s17, v223
	v_med3_f32 v70, v70, s17, v223
	v_med3_f32 v71, v71, s17, v223
	v_med3_f32 v72, v72, s17, v223
	v_med3_f32 v73, v73, s17, v223
	v_pk_mul_f32 v[24:25], v[74:75], s[30:31] op_sel_hi:[1,0]
	v_pk_mul_f32 v[26:27], v[76:77], s[30:31] op_sel_hi:[1,0]
	v_pk_mul_f32 v[28:29], v[66:67], s[30:31] op_sel_hi:[1,0]
	v_pk_mul_f32 v[30:31], v[68:69], s[30:31] op_sel_hi:[1,0]
	v_pk_mul_f32 v[24:25], v[24:25], s[34:35] op_sel_hi:[1,0]
	v_pk_mul_f32 v[26:27], v[26:27], s[34:35] op_sel_hi:[1,0]
	v_pk_mul_f32 v[28:29], v[28:29], s[34:35] op_sel_hi:[1,0]
	v_pk_mul_f32 v[30:31], v[30:31], s[34:35] op_sel_hi:[1,0]
	v_exp_f32_e32 v24, v24
	v_exp_f32_e32 v25, v25
	v_exp_f32_e32 v26, v26
	v_exp_f32_e32 v27, v27
	v_exp_f32_e32 v28, v28
	v_exp_f32_e32 v29, v29
	v_exp_f32_e32 v30, v30
	v_exp_f32_e32 v31, v31
	v_pk_add_f32 v[24:25], v[24:25], 1.0 op_sel_hi:[1,0]
	v_pk_add_f32 v[26:27], v[26:27], 1.0 op_sel_hi:[1,0]
	v_pk_add_f32 v[28:29], v[28:29], 1.0 op_sel_hi:[1,0]
	v_pk_add_f32 v[30:31], v[30:31], 1.0 op_sel_hi:[1,0]
	v_rcp_f32_e32 v24, v24
	v_rcp_f32_e32 v25, v25
	v_rcp_f32_e32 v26, v26
	v_rcp_f32_e32 v27, v27
	v_rcp_f32_e32 v28, v28
	v_rcp_f32_e32 v29, v29
	v_rcp_f32_e32 v30, v30
	v_rcp_f32_e32 v31, v31
	v_pk_add_f32 v[78:79], v[78:79], 1.0 op_sel_hi:[1,0]
	v_pk_add_f32 v[80:81], v[80:81], 1.0 op_sel_hi:[1,0]
	v_pk_add_f32 v[70:71], v[70:71], 1.0 op_sel_hi:[1,0]
	v_pk_add_f32 v[72:73], v[72:73], 1.0 op_sel_hi:[1,0]
	v_pk_mul_f32 v[74:75], v[74:75], v[24:25]
	v_pk_mul_f32 v[76:77], v[76:77], v[26:27]
	v_pk_mul_f32 v[66:67], v[66:67], v[28:29]
	v_pk_mul_f32 v[68:69], v[68:69], v[30:31]
	v_pk_mul_f32 v[74:75], v[78:79], v[74:75]
	v_pk_mul_f32 v[76:77], v[80:81], v[76:77]
	v_pk_mul_f32 v[66:67], v[70:71], v[66:67]
	v_pk_mul_f32 v[68:69], v[72:73], v[68:69]
	v_cvt_pk_fp8_f32 v32, v74, v75
	v_cvt_pk_fp8_f32 v33, v66, v67
	v_cvt_pk_fp8_f32 v32, v76, v77 op_sel:[0,0,1]
	v_cvt_pk_fp8_f32 v33, v68, v69 op_sel:[0,0,1]
	s_mov_b32 s36, 0x24000
	v_lshl_add_u64 v[22:23], v[18:19], 0, s[36:37]
	global_store_dwordx2 v[22:23], v[32:33], off
	v_pk_add_f32 v[58:59], v[58:59], v[206:207]
	v_pk_add_f32 v[60:61], v[60:61], v[208:209]
	v_pk_add_f32 v[50:51], v[50:51], v[216:217]
	v_pk_add_f32 v[52:53], v[52:53], v[218:219]
	v_pk_add_f32 v[62:63], v[62:63], v[224:225]
	v_pk_add_f32 v[64:65], v[64:65], v[226:227]
	v_pk_add_f32 v[54:55], v[54:55], v[228:229]
	v_pk_add_f32 v[56:57], v[56:57], v[230:231]
	v_min_f32_e32 v58, 0x40e00000, v58
	v_min_f32_e32 v59, 0x40e00000, v59
	v_min_f32_e32 v60, 0x40e00000, v60
	v_min_f32_e32 v61, 0x40e00000, v61
	v_min_f32_e32 v50, 0x40e00000, v50
	v_min_f32_e32 v51, 0x40e00000, v51
	v_min_f32_e32 v52, 0x40e00000, v52
	v_min_f32_e32 v53, 0x40e00000, v53
	v_med3_f32 v62, v62, s17, v223
	v_med3_f32 v63, v63, s17, v223
	v_med3_f32 v64, v64, s17, v223
	v_med3_f32 v65, v65, s17, v223
	v_med3_f32 v54, v54, s17, v223
	v_med3_f32 v55, v55, s17, v223
	v_med3_f32 v56, v56, s17, v223
	v_med3_f32 v57, v57, s17, v223
	v_pk_mul_f32 v[24:25], v[58:59], s[30:31] op_sel_hi:[1,0]
	v_pk_mul_f32 v[26:27], v[60:61], s[30:31] op_sel_hi:[1,0]
	v_pk_mul_f32 v[28:29], v[50:51], s[30:31] op_sel_hi:[1,0]
	v_pk_mul_f32 v[30:31], v[52:53], s[30:31] op_sel_hi:[1,0]
	v_pk_mul_f32 v[24:25], v[24:25], s[34:35] op_sel_hi:[1,0]
	v_pk_mul_f32 v[26:27], v[26:27], s[34:35] op_sel_hi:[1,0]
	v_pk_mul_f32 v[28:29], v[28:29], s[34:35] op_sel_hi:[1,0]
	v_pk_mul_f32 v[30:31], v[30:31], s[34:35] op_sel_hi:[1,0]
	v_exp_f32_e32 v24, v24
	v_exp_f32_e32 v25, v25
	v_exp_f32_e32 v26, v26
	v_exp_f32_e32 v27, v27
	v_exp_f32_e32 v28, v28
	v_exp_f32_e32 v29, v29
	v_exp_f32_e32 v30, v30
	v_exp_f32_e32 v31, v31
	v_pk_add_f32 v[24:25], v[24:25], 1.0 op_sel_hi:[1,0]
	v_pk_add_f32 v[26:27], v[26:27], 1.0 op_sel_hi:[1,0]
	v_pk_add_f32 v[28:29], v[28:29], 1.0 op_sel_hi:[1,0]
	v_pk_add_f32 v[30:31], v[30:31], 1.0 op_sel_hi:[1,0]
	v_rcp_f32_e32 v24, v24
	v_rcp_f32_e32 v25, v25
	v_rcp_f32_e32 v26, v26
	v_rcp_f32_e32 v27, v27
	v_rcp_f32_e32 v28, v28
	v_rcp_f32_e32 v29, v29
	v_rcp_f32_e32 v30, v30
	v_rcp_f32_e32 v31, v31
	v_pk_add_f32 v[62:63], v[62:63], 1.0 op_sel_hi:[1,0]
	v_pk_add_f32 v[64:65], v[64:65], 1.0 op_sel_hi:[1,0]
	v_pk_add_f32 v[54:55], v[54:55], 1.0 op_sel_hi:[1,0]
	v_pk_add_f32 v[56:57], v[56:57], 1.0 op_sel_hi:[1,0]
	v_pk_mul_f32 v[58:59], v[58:59], v[24:25]
	v_pk_mul_f32 v[60:61], v[60:61], v[26:27]
	v_pk_mul_f32 v[50:51], v[50:51], v[28:29]
	v_pk_mul_f32 v[52:53], v[52:53], v[30:31]
	v_pk_mul_f32 v[58:59], v[62:63], v[58:59]
	v_pk_mul_f32 v[60:61], v[64:65], v[60:61]
	v_pk_mul_f32 v[50:51], v[54:55], v[50:51]
	v_pk_mul_f32 v[52:53], v[56:57], v[52:53]
	v_cvt_pk_fp8_f32 v32, v58, v59
	v_cvt_pk_fp8_f32 v33, v50, v51
	v_cvt_pk_fp8_f32 v32, v60, v61 op_sel:[0,0,1]
	v_cvt_pk_fp8_f32 v33, v52, v53 op_sel:[0,0,1]
	s_mov_b32 s36, 0x28000
	v_lshl_add_u64 v[22:23], v[18:19], 0, s[36:37]
	global_store_dwordx2 v[22:23], v[32:33], off
	v_pk_add_f32 v[42:43], v[42:43], v[206:207]
	v_pk_add_f32 v[44:45], v[44:45], v[208:209]
	v_pk_add_f32 v[38:39], v[38:39], v[216:217]
	v_pk_add_f32 v[40:41], v[40:41], v[218:219]
	v_pk_add_f32 v[46:47], v[46:47], v[224:225]
	v_pk_add_f32 v[48:49], v[48:49], v[226:227]
	v_pk_add_f32 v[34:35], v[34:35], v[228:229]
	v_pk_add_f32 v[36:37], v[36:37], v[230:231]
	v_min_f32_e32 v42, 0x40e00000, v42
	v_min_f32_e32 v43, 0x40e00000, v43
	v_min_f32_e32 v44, 0x40e00000, v44
	v_min_f32_e32 v45, 0x40e00000, v45
	v_min_f32_e32 v38, 0x40e00000, v38
	v_min_f32_e32 v39, 0x40e00000, v39
	v_min_f32_e32 v40, 0x40e00000, v40
	v_min_f32_e32 v41, 0x40e00000, v41
	v_med3_f32 v46, v46, s17, v223
	v_med3_f32 v47, v47, s17, v223
	v_med3_f32 v48, v48, s17, v223
	v_med3_f32 v49, v49, s17, v223
	v_med3_f32 v34, v34, s17, v223
	v_med3_f32 v35, v35, s17, v223
	v_med3_f32 v36, v36, s17, v223
	v_med3_f32 v37, v37, s17, v223
	v_pk_mul_f32 v[24:25], v[42:43], s[30:31] op_sel_hi:[1,0]
	v_pk_mul_f32 v[26:27], v[44:45], s[30:31] op_sel_hi:[1,0]
	v_pk_mul_f32 v[28:29], v[38:39], s[30:31] op_sel_hi:[1,0]
	v_pk_mul_f32 v[30:31], v[40:41], s[30:31] op_sel_hi:[1,0]
	v_pk_mul_f32 v[24:25], v[24:25], s[34:35] op_sel_hi:[1,0]
	v_pk_mul_f32 v[26:27], v[26:27], s[34:35] op_sel_hi:[1,0]
	v_pk_mul_f32 v[28:29], v[28:29], s[34:35] op_sel_hi:[1,0]
	v_pk_mul_f32 v[30:31], v[30:31], s[34:35] op_sel_hi:[1,0]
	v_exp_f32_e32 v24, v24
	v_exp_f32_e32 v25, v25
	v_exp_f32_e32 v26, v26
	v_exp_f32_e32 v27, v27
	v_exp_f32_e32 v28, v28
	v_exp_f32_e32 v29, v29
	v_exp_f32_e32 v30, v30
	v_exp_f32_e32 v31, v31
	v_pk_add_f32 v[24:25], v[24:25], 1.0 op_sel_hi:[1,0]
	v_pk_add_f32 v[26:27], v[26:27], 1.0 op_sel_hi:[1,0]
	v_pk_add_f32 v[28:29], v[28:29], 1.0 op_sel_hi:[1,0]
	v_pk_add_f32 v[30:31], v[30:31], 1.0 op_sel_hi:[1,0]
	v_rcp_f32_e32 v24, v24
	v_rcp_f32_e32 v25, v25
	v_rcp_f32_e32 v26, v26
	v_rcp_f32_e32 v27, v27
	v_rcp_f32_e32 v28, v28
	v_rcp_f32_e32 v29, v29
	v_rcp_f32_e32 v30, v30
	v_rcp_f32_e32 v31, v31
	v_pk_add_f32 v[46:47], v[46:47], 1.0 op_sel_hi:[1,0]
	v_pk_add_f32 v[48:49], v[48:49], 1.0 op_sel_hi:[1,0]
	v_pk_add_f32 v[34:35], v[34:35], 1.0 op_sel_hi:[1,0]
	v_pk_add_f32 v[36:37], v[36:37], 1.0 op_sel_hi:[1,0]
	v_pk_mul_f32 v[42:43], v[42:43], v[24:25]
	v_pk_mul_f32 v[44:45], v[44:45], v[26:27]
	v_pk_mul_f32 v[38:39], v[38:39], v[28:29]
	v_pk_mul_f32 v[40:41], v[40:41], v[30:31]
	v_pk_mul_f32 v[42:43], v[46:47], v[42:43]
	v_pk_mul_f32 v[44:45], v[48:49], v[44:45]
	v_pk_mul_f32 v[38:39], v[34:35], v[38:39]
	v_pk_mul_f32 v[40:41], v[36:37], v[40:41]
	v_cvt_pk_fp8_f32 v32, v42, v43
	v_cvt_pk_fp8_f32 v33, v38, v39
	v_cvt_pk_fp8_f32 v32, v44, v45 op_sel:[0,0,1]
	v_cvt_pk_fp8_f32 v33, v40, v41 op_sel:[0,0,1]
	s_mov_b32 s36, 0x2c000
	v_lshl_add_u64 v[22:23], v[18:19], 0, s[36:37]
	s_mov_b32 s13, 0x28000
	s_and_b64 vcc, exec, s[22:23]
	global_store_dwordx2 v[22:23], v[32:33], off
	s_cbranch_vccz .LBB0_1222
	v_readlane_b32 s24, v253, 4
	v_readlane_b32 s26, v253, 6
	v_readlane_b32 s27, v253, 7
	v_readlane_b32 s25, v253, 5
	s_and_b64 vcc, exec, s[0:1]
	v_mov_b64_e32 v[36:37], s[26:27]
	v_mov_b64_e32 v[156:157], s[26:27]
	v_mov_b64_e32 v[148:149], s[26:27]
	v_mov_b64_e32 v[140:141], s[26:27]
	v_mov_b64_e32 v[132:133], s[26:27]
	v_mov_b64_e32 v[124:125], s[26:27]
	v_mov_b64_e32 v[116:117], s[26:27]
	v_mov_b64_e32 v[108:109], s[26:27]
	v_mov_b64_e32 v[100:101], s[26:27]
	v_mov_b64_e32 v[160:161], s[26:27]
	v_mov_b64_e32 v[152:153], s[26:27]
	v_mov_b64_e32 v[144:145], s[26:27]
	v_mov_b64_e32 v[136:137], s[26:27]
	v_mov_b64_e32 v[128:129], s[26:27]
	v_mov_b64_e32 v[120:121], s[26:27]
	v_mov_b64_e32 v[112:113], s[26:27]
	v_mov_b64_e32 v[104:105], s[26:27]
	v_mov_b64_e32 v[92:93], s[26:27]
	v_mov_b64_e32 v[84:85], s[26:27]
	v_mov_b64_e32 v[76:77], s[26:27]
	v_mov_b64_e32 v[68:69], s[26:27]
	v_mov_b64_e32 v[60:61], s[26:27]
	v_mov_b64_e32 v[52:53], s[26:27]
	v_mov_b64_e32 v[44:45], s[26:27]
	v_mov_b64_e32 v[40:41], s[26:27]
	v_mov_b64_e32 v[96:97], s[26:27]
	v_mov_b64_e32 v[88:89], s[26:27]
	v_mov_b64_e32 v[80:81], s[26:27]
	v_mov_b64_e32 v[72:73], s[26:27]
	v_mov_b64_e32 v[64:65], s[26:27]
	v_mov_b64_e32 v[56:57], s[26:27]
	v_mov_b64_e32 v[48:49], s[26:27]
	v_mov_b64_e32 v[34:35], s[24:25]
	v_mov_b64_e32 v[154:155], s[24:25]
	v_mov_b64_e32 v[146:147], s[24:25]
	v_mov_b64_e32 v[138:139], s[24:25]
	v_mov_b64_e32 v[130:131], s[24:25]
	v_mov_b64_e32 v[122:123], s[24:25]
	v_mov_b64_e32 v[114:115], s[24:25]
	v_mov_b64_e32 v[106:107], s[24:25]
	v_mov_b64_e32 v[98:99], s[24:25]
	v_mov_b64_e32 v[158:159], s[24:25]
	v_mov_b64_e32 v[150:151], s[24:25]
	v_mov_b64_e32 v[142:143], s[24:25]
	v_mov_b64_e32 v[134:135], s[24:25]
	v_mov_b64_e32 v[126:127], s[24:25]
	v_mov_b64_e32 v[118:119], s[24:25]
	v_mov_b64_e32 v[110:111], s[24:25]
	v_mov_b64_e32 v[102:103], s[24:25]
	v_mov_b64_e32 v[90:91], s[24:25]
	v_mov_b64_e32 v[82:83], s[24:25]
	v_mov_b64_e32 v[74:75], s[24:25]
	v_mov_b64_e32 v[66:67], s[24:25]
	v_mov_b64_e32 v[58:59], s[24:25]
	v_mov_b64_e32 v[50:51], s[24:25]
	v_mov_b64_e32 v[42:43], s[24:25]
	v_mov_b64_e32 v[38:39], s[24:25]
	v_mov_b64_e32 v[94:95], s[24:25]
	v_mov_b64_e32 v[86:87], s[24:25]
	v_mov_b64_e32 v[78:79], s[24:25]
	v_mov_b64_e32 v[70:71], s[24:25]
	v_mov_b64_e32 v[62:63], s[24:25]
	v_mov_b64_e32 v[54:55], s[24:25]
	v_mov_b64_e32 v[46:47], s[24:25]
	s_cbranch_vccz .LBB0_1221
	s_barrier
	s_branch .LBB0_1221
